# attention main loop: wave-half stagger (waves 4-7 barrier before exp block, K reads hoisted)
# baseline (speedup 1.0000x reference)
.LBB0_1700:
	s_cmp_lg_u32 0, -1
	s_waitcnt vmcnt(0) lgkmcnt(0)
	s_barrier
	s_cselect_b32 s9, 0, 0
	s_nop 8
	v_exp_f32_e32 v50, v2
	v_exp_f32_e32 v51, v3
	v_lshl_add_u64 v[2:3], v[214:215], 0, s[16:17]
	s_mov_b32 s8, m0
	s_mov_b32 m0, s50
	s_nop 0
	global_load_lds_dwordx4 v[2:3], off
	s_mov_b32 m0, s8
	s_add_i32 s9, s9, s30
	v_lshl_add_u64 v[216:217], v[34:35], 0, s[12:13]
	s_add_i32 s9, s9, 0x8000
	s_mov_b32 s30, m0
	s_mov_b32 m0, s9
	s_nop 0
	global_load_lds_dwordx4 v[216:217], off
	s_mov_b32 m0, s30
	ds_read_b128 v[174:177], v232 offset:8192
	ds_read_b128 v[166:169], v232 offset:8704
	ds_read_b128 v[170:173], v232 offset:10240
	ds_read_b128 v[158:161], v232 offset:10752
	ds_read_b128 v[162:165], v232 offset:12288
	ds_read_b128 v[150:153], v232 offset:12800
	ds_read_b128 v[154:157], v232 offset:14336
	ds_read_b128 v[146:149], v232 offset:14848
	v_exp_f32_e32 v66, v18
	v_exp_f32_e32 v67, v19
	v_exp_f32_e32 v68, v20
	v_exp_f32_e32 v69, v21
	v_exp_f32_e32 v70, v22
	v_exp_f32_e32 v71, v23
	v_exp_f32_e32 v72, v24
	v_exp_f32_e32 v73, v25
	v_exp_f32_e32 v74, v26
	v_exp_f32_e32 v75, v27
	v_exp_f32_e32 v76, v28
	v_exp_f32_e32 v77, v29
	v_exp_f32_e32 v78, v30
	v_exp_f32_e32 v79, v31
	v_exp_f32_e32 v80, v32
	v_exp_f32_e32 v81, v33
	v_exp_f32_e32 v52, v4
	v_exp_f32_e32 v53, v5
	v_exp_f32_e32 v54, v6
	v_exp_f32_e32 v55, v7
	v_exp_f32_e32 v56, v8
	v_exp_f32_e32 v57, v9
	v_exp_f32_e32 v58, v10
	v_exp_f32_e32 v59, v11
	v_exp_f32_e32 v60, v12
	v_exp_f32_e32 v61, v13
	v_exp_f32_e32 v62, v14
	v_exp_f32_e32 v63, v15
	v_exp_f32_e32 v64, v16
	v_exp_f32_e32 v65, v17
	s_waitcnt vmcnt(2) lgkmcnt(0)
	s_barrier
	s_mov_b32 s8, 0
	s_cmp_lt_i32 s49, 7
	s_mov_b32 s42, 0
	s_cbranch_scc1 .LBB0_1741
	v_lshl_add_u64 v[218:219], v[34:35], 0, s[16:17]
	v_mov_b32_e32 v34, 0
	s_add_i32 s9, s49, -5
	v_lshl_add_u64 v[220:221], v[214:215], 0, s[18:19]
	s_mov_b32 s30, 1
	s_movk_i32 s53, 0x4000
	s_movk_i32 s52, 0x2000
	v_mov_b32_e32 v35, v241
	v_mov_b32_e32 v2, 0
	v_mov_b32_e32 v3, v34
	v_mov_b32_e32 v4, v34
	v_mov_b32_e32 v5, v34
	v_mov_b32_e32 v6, v34
	v_mov_b32_e32 v7, v34
	v_mov_b32_e32 v8, v34
	v_mov_b32_e32 v9, v34
	v_mov_b32_e32 v10, v34
	v_mov_b32_e32 v11, v34
	v_mov_b32_e32 v12, v34
	v_mov_b32_e32 v13, v34
	v_mov_b32_e32 v14, v34
	v_mov_b32_e32 v15, v34
	v_mov_b32_e32 v16, v34
	v_mov_b32_e32 v17, v34
	v_mov_b32_e32 v18, 0
	v_mov_b32_e32 v19, v34
	v_mov_b32_e32 v20, v34
	v_mov_b32_e32 v21, v34
	v_mov_b32_e32 v22, v34
	v_mov_b32_e32 v23, v34
	v_mov_b32_e32 v24, v34
	v_mov_b32_e32 v25, v34
	v_mov_b32_e32 v26, v34
	v_mov_b32_e32 v27, v34
	v_mov_b32_e32 v28, v34
	v_mov_b32_e32 v29, v34
	v_mov_b32_e32 v30, v34
	v_mov_b32_e32 v31, v34
	v_mov_b32_e32 v32, v34
	v_mov_b32_e32 v33, v34
	s_cmp_gt_u32 s48, 3
	s_cbranch_scc1 .Lattn_g2_loop
.LBB0_1702:
	s_mov_b32 s8, s53
	s_mov_b32 s41, s52
	ds_read_b128 v[36:39], v35
	ds_read_b128 v[40:43], v35 offset:32
	ds_read_b128 v[44:47], v35 offset:64
	ds_read_b128 v[82:85], v35 offset:96
	ds_read_b128 v[178:181], v35 offset:128
	ds_read_b128 v[86:89], v35 offset:160
	ds_read_b128 v[90:93], v35 offset:192
	ds_read_b128 v[94:97], v35 offset:224
	s_waitcnt lgkmcnt(4)
	v_sub_f32_e32 v113, v213, v85
	v_sub_f32_e32 v112, v213, v84
	v_sub_f32_e32 v111, v213, v83
	v_sub_f32_e32 v110, v213, v82
	v_sub_f32_e32 v109, v213, v47
	v_sub_f32_e32 v108, v213, v46
	v_sub_f32_e32 v107, v213, v45
	v_sub_f32_e32 v106, v213, v44
	v_sub_f32_e32 v105, v213, v43
	v_sub_f32_e32 v104, v213, v42
	v_sub_f32_e32 v103, v213, v41
	v_sub_f32_e32 v102, v213, v40
	v_sub_f32_e32 v101, v213, v39
	v_sub_f32_e32 v100, v213, v38
	v_sub_f32_e32 v99, v213, v37
	v_sub_f32_e32 v98, v213, v36
	s_waitcnt lgkmcnt(0)
	v_sub_f32_e32 v97, v213, v97
	v_sub_f32_e32 v96, v213, v96
	v_sub_f32_e32 v95, v213, v95
	v_sub_f32_e32 v94, v213, v94
	v_sub_f32_e32 v93, v213, v93
	v_sub_f32_e32 v92, v213, v92
	v_sub_f32_e32 v91, v213, v91
	v_sub_f32_e32 v90, v213, v90
	v_sub_f32_e32 v89, v213, v89
	v_sub_f32_e32 v88, v213, v88
	v_sub_f32_e32 v87, v213, v87
	v_sub_f32_e32 v86, v213, v86
	v_sub_f32_e32 v85, v213, v181
	v_sub_f32_e32 v84, v213, v180
	v_sub_f32_e32 v83, v213, v179
	v_sub_f32_e32 v82, v213, v178
	v_add_u32_e32 v178, s42, v235
	ds_read_b64_tr_b16 v[36:37], v178 offset:24576
	ds_read_b64_tr_b16 v[38:39], v178 offset:25088
	v_add_f32_e32 v40, v66, v67
	v_add_f32_e32 v40, v68, v40
	v_add_f32_e32 v40, v69, v40
	v_add_f32_e32 v40, v70, v40
	v_add_f32_e32 v44, v71, v40
	v_cvt_pk_bf16_f32 v130, v66, v67
	v_cvt_pk_bf16_f32 v131, v68, v69
	v_mfma_f32_32x32x16_bf16 v[98:113], v[174:177], v[114:117], v[98:113]
	ds_read_b64_tr_b16 v[40:41], v178 offset:28672
	ds_read_b64_tr_b16 v[42:43], v178 offset:29184
	v_add_f32_e32 v44, v72, v44
	v_add_f32_e32 v44, v73, v44
	v_add_f32_e32 v44, v74, v44
	v_add_f32_e32 v48, v75, v44
	v_cvt_pk_bf16_f32 v132, v70, v71
	v_cvt_pk_bf16_f32 v133, v72, v73
	v_mfma_f32_32x32x16_bf16 v[82:97], v[166:169], v[114:117], v[82:97]
	ds_read_b64_tr_b16 v[44:45], v178 offset:25600
	ds_read_b64_tr_b16 v[46:47], v178 offset:26112
	v_add_f32_e32 v48, v76, v48
	v_add_f32_e32 v48, v77, v48
	v_add_f32_e32 v48, v78, v48
	v_add_f32_e32 v48, v79, v48
	v_cvt_pk_bf16_f32 v134, v74, v75
	v_cvt_pk_bf16_f32 v135, v76, v77
	v_mfma_f32_32x32x16_bf16 v[98:113], v[170:173], v[118:121], v[98:113]
	ds_read_b64_tr_b16 v[66:67], v178 offset:29696
	ds_read_b64_tr_b16 v[68:69], v178 offset:30208
	v_add_f32_e32 v48, v80, v48
	v_add_f32_e32 v48, v81, v48
	v_add_f32_e32 v48, v50, v48
	v_add_f32_e32 v48, v51, v48
	v_cvt_pk_bf16_f32 v136, v78, v79
	v_cvt_pk_bf16_f32 v137, v80, v81
	v_mfma_f32_32x32x16_bf16 v[82:97], v[158:161], v[118:121], v[82:97]
	ds_read_b64_tr_b16 v[158:159], v178 offset:26624
	ds_read_b64_tr_b16 v[160:161], v178 offset:27136
	v_add_f32_e32 v48, v52, v48
	v_add_f32_e32 v48, v53, v48
	v_add_f32_e32 v48, v54, v48
	v_add_f32_e32 v70, v55, v48
	v_cvt_pk_bf16_f32 v138, v50, v51
	v_cvt_pk_bf16_f32 v139, v52, v53
	v_mfma_f32_32x32x16_bf16 v[98:113], v[162:165], v[122:125], v[98:113]
	ds_read_b64_tr_b16 v[48:49], v178 offset:30720
	ds_read_b64_tr_b16 v[50:51], v178 offset:31232
	v_add_f32_e32 v52, v56, v70
	v_add_f32_e32 v52, v57, v52
	v_add_f32_e32 v52, v58, v52
	v_add_f32_e32 v52, v59, v52
	v_cvt_pk_bf16_f32 v140, v54, v55
	v_cvt_pk_bf16_f32 v141, v56, v57
	v_mfma_f32_32x32x16_bf16 v[82:97], v[150:153], v[122:125], v[82:97]
	ds_read_b64_tr_b16 v[150:151], v178 offset:27648
	ds_read_b64_tr_b16 v[152:153], v178 offset:28160
	v_add_f32_e32 v52, v60, v52
	v_add_f32_e32 v52, v61, v52
	v_add_f32_e32 v52, v62, v52
	v_add_f32_e32 v52, v63, v52
	v_cvt_pk_bf16_f32 v142, v58, v59
	v_cvt_pk_bf16_f32 v143, v60, v61
	v_mfma_f32_32x32x16_bf16 v[98:113], v[154:157], v[126:129], v[98:113]
	ds_read_b64_tr_b16 v[166:167], v178 offset:31744
	ds_read_b64_tr_b16 v[168:169], v178 offset:32256
	v_add_f32_e32 v52, v64, v52
	v_add_f32_e32 v52, v65, v52
	v_add_f32_e32 v251, 0, v52
	v_cvt_pk_bf16_f32 v144, v62, v63
	v_cvt_pk_bf16_f32 v145, v64, v65
	v_mfma_f32_32x32x16_bf16 v[82:97], v[146:149], v[126:129], v[82:97]
	v_lshl_add_u64 v[52:53], v[220:221], 0, s[20:21]
	s_add_i32 s42, s52, s50
	s_mov_b32 s43, m0
	s_mov_b32 m0, s42
	s_nop 0
	global_load_lds_dwordx4 v[52:53], off
	s_mov_b32 m0, s43
	v_lshl_add_u64 v[52:53], v[218:219], 0, s[20:21]
	s_add_i32 s42, s53, s51
	s_mov_b32 s43, m0
	s_mov_b32 m0, s42
	s_nop 0
	global_load_lds_dwordx4 v[52:53], off
	s_mov_b32 m0, s43
	v_exp_f32_e32 v98, v98
	v_exp_f32_e32 v99, v99
	v_exp_f32_e32 v100, v100
	v_exp_f32_e32 v101, v101
	s_nop 0
	v_exp_f32_e32 v102, v102
	v_exp_f32_e32 v103, v103
	v_exp_f32_e32 v104, v104
	v_exp_f32_e32 v105, v105
	v_add_u32_e32 v52, s8, v232
	ds_read_b128 v[186:189], v52
	ds_read_b128 v[178:181], v52 offset:512
	v_exp_f32_e32 v106, v106
	v_exp_f32_e32 v107, v107
	v_exp_f32_e32 v108, v108
	v_exp_f32_e32 v109, v109
	ds_read_b128 v[182:185], v52 offset:2048
	ds_read_b128 v[170:173], v52 offset:2560
	v_exp_f32_e32 v110, v110
	v_exp_f32_e32 v111, v111
	v_exp_f32_e32 v112, v112
	v_exp_f32_e32 v113, v113
	ds_read_b128 v[174:177], v52 offset:4096
	ds_read_b128 v[154:157], v52 offset:4608
	v_exp_f32_e32 v82, v82
	v_exp_f32_e32 v83, v83
	v_exp_f32_e32 v84, v84
	v_exp_f32_e32 v85, v85
	ds_read_b128 v[162:165], v52 offset:6144
	ds_read_b128 v[146:149], v52 offset:6656
	v_exp_f32_e32 v86, v86
	v_exp_f32_e32 v87, v87
	v_exp_f32_e32 v88, v88
	v_exp_f32_e32 v89, v89
	s_nop 0
	v_exp_f32_e32 v90, v90
	v_exp_f32_e32 v91, v91
	v_exp_f32_e32 v92, v92
	v_exp_f32_e32 v93, v93
	s_nop 0
	v_exp_f32_e32 v94, v94
	v_exp_f32_e32 v95, v95
	v_exp_f32_e32 v96, v96
	v_exp_f32_e32 v97, v97
	s_waitcnt vmcnt(2) lgkmcnt(0)
	s_barrier
	s_add_i32 s42, s53, 0x2000
	s_waitcnt lgkmcnt(14)
	v_mfma_f32_32x32x16_bf16 v[2:17], v[130:133], v[36:39], v[2:17]
	s_cmpk_lg_i32 s53, 0x4000
	v_add_f32_e32 v34, v34, v251
	s_cselect_b32 s52, s42, 0
	v_mfma_f32_32x32x16_bf16 v[18:33], v[130:133], v[40:43], v[18:33]
	ds_read_b128 v[36:39], v35 offset:256
	ds_read_b128 v[40:43], v35 offset:288
	ds_read_b128 v[52:55], v35 offset:320
	ds_read_b128 v[56:59], v35 offset:352
	ds_read_b128 v[242:245], v35 offset:384
	ds_read_b128 v[246:249], v35 offset:416
	ds_read_b128 v[190:193], v35 offset:448
	ds_read_b128 v[60:63], v35 offset:480
	s_waitcnt lgkmcnt(4)
	v_sub_f32_e32 v81, v213, v59
	v_sub_f32_e32 v80, v213, v58
	v_sub_f32_e32 v79, v213, v57
	v_sub_f32_e32 v78, v213, v56
	v_sub_f32_e32 v77, v213, v55
	v_sub_f32_e32 v76, v213, v54
	v_mfma_f32_32x32x16_bf16 v[2:17], v[134:137], v[44:47], v[2:17]
	v_sub_f32_e32 v75, v213, v53
	v_sub_f32_e32 v74, v213, v52
	v_sub_f32_e32 v73, v213, v43
	v_sub_f32_e32 v72, v213, v42
	v_sub_f32_e32 v71, v213, v41
	v_sub_f32_e32 v70, v213, v40
	s_waitcnt lgkmcnt(0)
	v_sub_f32_e32 v65, v213, v63
	v_mfma_f32_32x32x16_bf16 v[18:33], v[134:137], v[66:69], v[18:33]
	v_sub_f32_e32 v69, v213, v39
	v_sub_f32_e32 v68, v213, v38
	v_sub_f32_e32 v67, v213, v37
	v_sub_f32_e32 v66, v213, v36
	v_sub_f32_e32 v64, v213, v62
	v_sub_f32_e32 v63, v213, v61
	v_sub_f32_e32 v62, v213, v60
	v_mfma_f32_32x32x16_bf16 v[2:17], v[138:141], v[158:161], v[2:17]
	v_sub_f32_e32 v61, v213, v193
	v_sub_f32_e32 v60, v213, v192
	v_sub_f32_e32 v59, v213, v191
	v_sub_f32_e32 v58, v213, v190
	v_sub_f32_e32 v57, v213, v249
	v_sub_f32_e32 v56, v213, v248
	v_sub_f32_e32 v55, v213, v247
	v_mfma_f32_32x32x16_bf16 v[18:33], v[138:141], v[48:51], v[18:33]
	v_sub_f32_e32 v54, v213, v246
	v_sub_f32_e32 v53, v213, v245
	v_sub_f32_e32 v52, v213, v244
	v_sub_f32_e32 v51, v213, v243
	v_sub_f32_e32 v50, v213, v242
	v_mfma_f32_32x32x16_bf16 v[2:17], v[142:145], v[150:153], v[2:17]
	v_mfma_f32_32x32x16_bf16 v[18:33], v[142:145], v[166:169], v[18:33]
	v_add_u32_e32 v48, s41, v235
	ds_read_b64_tr_b16 v[36:37], v48 offset:24576
	ds_read_b64_tr_b16 v[38:39], v48 offset:25088
	v_mfma_f32_32x32x16_bf16 v[66:81], v[186:189], v[114:117], v[66:81]
	v_add_f32_e32 v40, v98, v99
	v_add_f32_e32 v40, v100, v40
	v_add_f32_e32 v40, v101, v40
	v_add_f32_e32 v40, v102, v40
	v_add_f32_e32 v44, v103, v40
	v_cvt_pk_bf16_f32 v130, v98, v99
	v_cvt_pk_bf16_f32 v131, v100, v101
	ds_read_b64_tr_b16 v[40:41], v48 offset:28672
	ds_read_b64_tr_b16 v[42:43], v48 offset:29184
	v_mfma_f32_32x32x16_bf16 v[50:65], v[178:181], v[114:117], v[50:65]
	v_add_f32_e32 v44, v104, v44
	v_add_f32_e32 v44, v105, v44
	v_add_f32_e32 v44, v106, v44
	v_add_f32_e32 v49, v107, v44
	v_cvt_pk_bf16_f32 v132, v102, v103
	v_cvt_pk_bf16_f32 v133, v104, v105
	ds_read_b64_tr_b16 v[44:45], v48 offset:25600
	ds_read_b64_tr_b16 v[46:47], v48 offset:26112
	v_mfma_f32_32x32x16_bf16 v[66:81], v[182:185], v[118:121], v[66:81]
	v_add_f32_e32 v49, v108, v49
	v_add_f32_e32 v49, v109, v49
	v_add_f32_e32 v49, v110, v49
	v_add_f32_e32 v49, v111, v49
	v_cvt_pk_bf16_f32 v134, v106, v107
	v_cvt_pk_bf16_f32 v135, v108, v109
	ds_read_b64_tr_b16 v[98:99], v48 offset:29696
	ds_read_b64_tr_b16 v[100:101], v48 offset:30208
	v_mfma_f32_32x32x16_bf16 v[50:65], v[170:173], v[118:121], v[50:65]
	v_add_f32_e32 v49, v112, v49
	v_add_f32_e32 v49, v113, v49
	v_add_f32_e32 v49, v82, v49
	v_add_f32_e32 v49, v83, v49
	v_cvt_pk_bf16_f32 v136, v110, v111
	v_cvt_pk_bf16_f32 v137, v112, v113
	ds_read_b64_tr_b16 v[102:103], v48 offset:26624
	ds_read_b64_tr_b16 v[104:105], v48 offset:27136
	v_mfma_f32_32x32x16_bf16 v[66:81], v[174:177], v[122:125], v[66:81]
	v_add_f32_e32 v49, v84, v49
	v_add_f32_e32 v49, v85, v49
	v_add_f32_e32 v49, v86, v49
	v_add_f32_e32 v49, v87, v49
	v_cvt_pk_bf16_f32 v138, v82, v83
	v_cvt_pk_bf16_f32 v139, v84, v85
	ds_read_b64_tr_b16 v[82:83], v48 offset:30720
	ds_read_b64_tr_b16 v[84:85], v48 offset:31232
	v_mfma_f32_32x32x16_bf16 v[50:65], v[154:157], v[122:125], v[50:65]
	v_add_f32_e32 v49, v88, v49
	v_add_f32_e32 v49, v89, v49
	v_add_f32_e32 v49, v90, v49
	v_add_f32_e32 v49, v91, v49
	v_cvt_pk_bf16_f32 v140, v86, v87
	v_cvt_pk_bf16_f32 v141, v88, v89
	ds_read_b64_tr_b16 v[86:87], v48 offset:27648
	ds_read_b64_tr_b16 v[88:89], v48 offset:28160
	v_mfma_f32_32x32x16_bf16 v[66:81], v[162:165], v[126:129], v[66:81]
	v_add_f32_e32 v49, v92, v49
	v_add_f32_e32 v49, v93, v49
	v_add_f32_e32 v49, v94, v49
	v_add_f32_e32 v49, v95, v49
	v_cvt_pk_bf16_f32 v142, v90, v91
	v_cvt_pk_bf16_f32 v143, v92, v93
	ds_read_b64_tr_b16 v[90:91], v48 offset:31744
	ds_read_b64_tr_b16 v[92:93], v48 offset:32256
	v_mfma_f32_32x32x16_bf16 v[50:65], v[146:149], v[126:129], v[50:65]
	v_add_f32_e32 v48, v96, v49
	v_add_f32_e32 v48, v97, v48
	v_add_f32_e32 v48, 0, v48
	v_cvt_pk_bf16_f32 v144, v94, v95
	v_cvt_pk_bf16_f32 v145, v96, v97
	s_add_i32 s41, s53, s50
	s_mov_b32 s42, m0
	s_mov_b32 m0, s41
	s_nop 0
	global_load_lds_dwordx4 v[220:221], off
	s_mov_b32 m0, s42
	s_add_i32 s41, s52, s51
	s_mov_b32 s42, m0
	s_mov_b32 m0, s41
	s_nop 0
	global_load_lds_dwordx4 v[218:219], off
	s_mov_b32 m0, s42
	v_add_f32_e32 v34, v34, v48
	s_add_i32 s30, s30, 2
	s_waitcnt lgkmcnt(14)
	v_mfma_f32_32x32x16_bf16 v[2:17], v[130:133], v[36:39], v[2:17]
	v_exp_f32_e32 v66, v66
	v_exp_f32_e32 v67, v67
	v_exp_f32_e32 v68, v68
	v_exp_f32_e32 v69, v69
	s_waitcnt lgkmcnt(12)
	v_mfma_f32_32x32x16_bf16 v[18:33], v[130:133], v[40:43], v[18:33]
	v_exp_f32_e32 v70, v70
	v_exp_f32_e32 v71, v71
	v_exp_f32_e32 v72, v72
	v_exp_f32_e32 v73, v73
	v_add_u32_e32 v36, s52, v232
	ds_read_b128 v[174:177], v36
	ds_read_b128 v[166:169], v36 offset:512
	s_waitcnt lgkmcnt(12)
	v_mfma_f32_32x32x16_bf16 v[2:17], v[134:137], v[44:47], v[2:17]
	v_exp_f32_e32 v74, v74
	v_exp_f32_e32 v75, v75
	v_exp_f32_e32 v76, v76
	v_exp_f32_e32 v77, v77
	ds_read_b128 v[170:173], v36 offset:2048
	ds_read_b128 v[158:161], v36 offset:2560
	s_waitcnt lgkmcnt(12)
	v_mfma_f32_32x32x16_bf16 v[18:33], v[134:137], v[98:101], v[18:33]
	v_exp_f32_e32 v78, v78
	v_exp_f32_e32 v79, v79
	v_exp_f32_e32 v80, v80
	v_exp_f32_e32 v81, v81
	ds_read_b128 v[162:165], v36 offset:4096
	ds_read_b128 v[150:153], v36 offset:4608
	s_waitcnt lgkmcnt(12)
	v_mfma_f32_32x32x16_bf16 v[2:17], v[138:141], v[102:105], v[2:17]
	v_exp_f32_e32 v50, v50
	v_exp_f32_e32 v51, v51
	v_exp_f32_e32 v52, v52
	v_exp_f32_e32 v53, v53
	ds_read_b128 v[154:157], v36 offset:6144
	ds_read_b128 v[146:149], v36 offset:6656
	s_waitcnt lgkmcnt(12)
	v_mfma_f32_32x32x16_bf16 v[18:33], v[138:141], v[82:85], v[18:33]
	v_exp_f32_e32 v54, v54
	v_exp_f32_e32 v55, v55
	v_exp_f32_e32 v56, v56
	v_exp_f32_e32 v57, v57
	s_waitcnt lgkmcnt(10)
	v_mfma_f32_32x32x16_bf16 v[2:17], v[142:145], v[86:89], v[2:17]
	v_exp_f32_e32 v58, v58
	v_exp_f32_e32 v59, v59
	v_exp_f32_e32 v60, v60
	v_exp_f32_e32 v61, v61
	s_waitcnt lgkmcnt(8)
	v_mfma_f32_32x32x16_bf16 v[18:33], v[142:145], v[90:93], v[18:33]
	v_exp_f32_e32 v62, v62
	v_exp_f32_e32 v63, v63
	v_exp_f32_e32 v64, v64
	v_exp_f32_e32 v65, v65
	s_waitcnt vmcnt(2) lgkmcnt(0)
	s_barrier
	s_add_i32 s41, s52, 0x2000
	s_cmpk_lg_i32 s52, 0x4000
	s_cselect_b32 s53, s41, 0
	v_lshl_add_u64 v[218:219], v[218:219], 0, s[14:15]
	v_lshl_add_u64 v[220:221], v[220:221], 0, s[14:15]
	v_add_u32_e32 v35, 0x200, v35
	s_cmp_ge_i32 s30, s9
	s_mov_b32 s42, s8
	s_cbranch_scc0 .LBB0_1702
	s_branch .Lattn_join
.Lattn_g2_loop:
	s_mov_b32 s8, s53
	s_mov_b32 s41, s52
	ds_read_b128 v[36:39], v35
	ds_read_b128 v[40:43], v35 offset:32
	ds_read_b128 v[44:47], v35 offset:64
	ds_read_b128 v[82:85], v35 offset:96
	ds_read_b128 v[178:181], v35 offset:128
	ds_read_b128 v[86:89], v35 offset:160
	ds_read_b128 v[90:93], v35 offset:192
	ds_read_b128 v[94:97], v35 offset:224
	s_waitcnt lgkmcnt(4)
	v_sub_f32_e32 v113, v213, v85
	v_sub_f32_e32 v112, v213, v84
	v_sub_f32_e32 v111, v213, v83
	v_sub_f32_e32 v110, v213, v82
	v_sub_f32_e32 v109, v213, v47
	v_sub_f32_e32 v108, v213, v46
	v_sub_f32_e32 v107, v213, v45
	v_sub_f32_e32 v106, v213, v44
	v_sub_f32_e32 v105, v213, v43
	v_sub_f32_e32 v104, v213, v42
	v_sub_f32_e32 v103, v213, v41
	v_sub_f32_e32 v102, v213, v40
	v_sub_f32_e32 v101, v213, v39
	v_sub_f32_e32 v100, v213, v38
	v_sub_f32_e32 v99, v213, v37
	v_sub_f32_e32 v98, v213, v36
	s_waitcnt lgkmcnt(0)
	v_sub_f32_e32 v97, v213, v97
	v_sub_f32_e32 v96, v213, v96
	v_sub_f32_e32 v95, v213, v95
	v_sub_f32_e32 v94, v213, v94
	v_sub_f32_e32 v93, v213, v93
	v_sub_f32_e32 v92, v213, v92
	v_sub_f32_e32 v91, v213, v91
	v_sub_f32_e32 v90, v213, v90
	v_sub_f32_e32 v89, v213, v89
	v_sub_f32_e32 v88, v213, v88
	v_sub_f32_e32 v87, v213, v87
	v_sub_f32_e32 v86, v213, v86
	v_sub_f32_e32 v85, v213, v181
	v_sub_f32_e32 v84, v213, v180
	v_sub_f32_e32 v83, v213, v179
	v_sub_f32_e32 v82, v213, v178
	v_add_u32_e32 v178, s42, v235
	ds_read_b64_tr_b16 v[36:37], v178 offset:24576
	ds_read_b64_tr_b16 v[38:39], v178 offset:25088
	v_add_f32_e32 v40, v66, v67
	v_add_f32_e32 v40, v68, v40
	v_add_f32_e32 v40, v69, v40
	v_add_f32_e32 v40, v70, v40
	v_add_f32_e32 v44, v71, v40
	v_cvt_pk_bf16_f32 v130, v66, v67
	v_cvt_pk_bf16_f32 v131, v68, v69
	v_mfma_f32_32x32x16_bf16 v[98:113], v[174:177], v[114:117], v[98:113]
	ds_read_b64_tr_b16 v[40:41], v178 offset:28672
	ds_read_b64_tr_b16 v[42:43], v178 offset:29184
	v_add_f32_e32 v44, v72, v44
	v_add_f32_e32 v44, v73, v44
	v_add_f32_e32 v44, v74, v44
	v_add_f32_e32 v48, v75, v44
	v_cvt_pk_bf16_f32 v132, v70, v71
	v_cvt_pk_bf16_f32 v133, v72, v73
	v_mfma_f32_32x32x16_bf16 v[82:97], v[166:169], v[114:117], v[82:97]
	ds_read_b64_tr_b16 v[44:45], v178 offset:25600
	ds_read_b64_tr_b16 v[46:47], v178 offset:26112
	v_add_f32_e32 v48, v76, v48
	v_add_f32_e32 v48, v77, v48
	v_add_f32_e32 v48, v78, v48
	v_add_f32_e32 v48, v79, v48
	v_cvt_pk_bf16_f32 v134, v74, v75
	v_cvt_pk_bf16_f32 v135, v76, v77
	v_mfma_f32_32x32x16_bf16 v[98:113], v[170:173], v[118:121], v[98:113]
	ds_read_b64_tr_b16 v[66:67], v178 offset:29696
	ds_read_b64_tr_b16 v[68:69], v178 offset:30208
	v_add_f32_e32 v48, v80, v48
	v_add_f32_e32 v48, v81, v48
	v_add_f32_e32 v48, v50, v48
	v_add_f32_e32 v48, v51, v48
	v_cvt_pk_bf16_f32 v136, v78, v79
	v_cvt_pk_bf16_f32 v137, v80, v81
	v_mfma_f32_32x32x16_bf16 v[82:97], v[158:161], v[118:121], v[82:97]
	ds_read_b64_tr_b16 v[158:159], v178 offset:26624
	ds_read_b64_tr_b16 v[160:161], v178 offset:27136
	v_add_f32_e32 v48, v52, v48
	v_add_f32_e32 v48, v53, v48
	v_add_f32_e32 v48, v54, v48
	v_add_f32_e32 v70, v55, v48
	v_cvt_pk_bf16_f32 v138, v50, v51
	v_cvt_pk_bf16_f32 v139, v52, v53
	v_mfma_f32_32x32x16_bf16 v[98:113], v[162:165], v[122:125], v[98:113]
	ds_read_b64_tr_b16 v[48:49], v178 offset:30720
	ds_read_b64_tr_b16 v[50:51], v178 offset:31232
	v_add_f32_e32 v52, v56, v70
	v_add_f32_e32 v52, v57, v52
	v_add_f32_e32 v52, v58, v52
	v_add_f32_e32 v52, v59, v52
	v_cvt_pk_bf16_f32 v140, v54, v55
	v_cvt_pk_bf16_f32 v141, v56, v57
	v_mfma_f32_32x32x16_bf16 v[82:97], v[150:153], v[122:125], v[82:97]
	ds_read_b64_tr_b16 v[150:151], v178 offset:27648
	ds_read_b64_tr_b16 v[152:153], v178 offset:28160
	v_add_f32_e32 v52, v60, v52
	v_add_f32_e32 v52, v61, v52
	v_add_f32_e32 v52, v62, v52
	v_add_f32_e32 v52, v63, v52
	v_cvt_pk_bf16_f32 v142, v58, v59
	v_cvt_pk_bf16_f32 v143, v60, v61
	v_mfma_f32_32x32x16_bf16 v[98:113], v[154:157], v[126:129], v[98:113]
	ds_read_b64_tr_b16 v[166:167], v178 offset:31744
	ds_read_b64_tr_b16 v[168:169], v178 offset:32256
	v_add_f32_e32 v52, v64, v52
	v_add_f32_e32 v52, v65, v52
	v_add_f32_e32 v251, 0, v52
	v_cvt_pk_bf16_f32 v144, v62, v63
	v_cvt_pk_bf16_f32 v145, v64, v65
	v_mfma_f32_32x32x16_bf16 v[82:97], v[146:149], v[126:129], v[82:97]
	v_lshl_add_u64 v[52:53], v[220:221], 0, s[20:21]
	s_add_i32 s42, s52, s50
	s_mov_b32 s43, m0
	s_mov_b32 m0, s42
	s_nop 0
	global_load_lds_dwordx4 v[52:53], off
	s_mov_b32 m0, s43
	v_lshl_add_u64 v[52:53], v[218:219], 0, s[20:21]
	s_add_i32 s42, s53, s51
	s_mov_b32 s43, m0
	s_mov_b32 m0, s42
	s_nop 0
	global_load_lds_dwordx4 v[52:53], off
	s_mov_b32 m0, s43
	v_add_u32_e32 v52, s8, v232
	ds_read_b128 v[186:189], v52
	ds_read_b128 v[178:181], v52 offset:512
	ds_read_b128 v[182:185], v52 offset:2048
	ds_read_b128 v[170:173], v52 offset:2560
	ds_read_b128 v[174:177], v52 offset:4096
	ds_read_b128 v[154:157], v52 offset:4608
	ds_read_b128 v[162:165], v52 offset:6144
	ds_read_b128 v[146:149], v52 offset:6656
	s_waitcnt vmcnt(2) lgkmcnt(0)
	s_barrier
	v_exp_f32_e32 v98, v98
	v_exp_f32_e32 v99, v99
	v_exp_f32_e32 v100, v100
	v_exp_f32_e32 v101, v101
	v_exp_f32_e32 v102, v102
	v_exp_f32_e32 v103, v103
	v_exp_f32_e32 v104, v104
	v_exp_f32_e32 v105, v105
	v_exp_f32_e32 v106, v106
	v_exp_f32_e32 v107, v107
	v_exp_f32_e32 v108, v108
	v_exp_f32_e32 v109, v109
	v_exp_f32_e32 v110, v110
	v_exp_f32_e32 v111, v111
	v_exp_f32_e32 v112, v112
	v_exp_f32_e32 v113, v113
	v_exp_f32_e32 v82, v82
	v_exp_f32_e32 v83, v83
	v_exp_f32_e32 v84, v84
	v_exp_f32_e32 v85, v85
	v_exp_f32_e32 v86, v86
	v_exp_f32_e32 v87, v87
	v_exp_f32_e32 v88, v88
	v_exp_f32_e32 v89, v89
	v_exp_f32_e32 v90, v90
	v_exp_f32_e32 v91, v91
	v_exp_f32_e32 v92, v92
	v_exp_f32_e32 v93, v93
	v_exp_f32_e32 v94, v94
	v_exp_f32_e32 v95, v95
	v_exp_f32_e32 v96, v96
	v_exp_f32_e32 v97, v97
	s_add_i32 s42, s53, 0x2000
	s_waitcnt lgkmcnt(14)
	v_mfma_f32_32x32x16_bf16 v[2:17], v[130:133], v[36:39], v[2:17]
	s_cmpk_lg_i32 s53, 0x4000
	v_add_f32_e32 v34, v34, v251
	s_cselect_b32 s52, s42, 0
	v_mfma_f32_32x32x16_bf16 v[18:33], v[130:133], v[40:43], v[18:33]
	ds_read_b128 v[36:39], v35 offset:256
	ds_read_b128 v[40:43], v35 offset:288
	ds_read_b128 v[52:55], v35 offset:320
	ds_read_b128 v[56:59], v35 offset:352
	ds_read_b128 v[242:245], v35 offset:384
	ds_read_b128 v[246:249], v35 offset:416
	ds_read_b128 v[190:193], v35 offset:448
	ds_read_b128 v[60:63], v35 offset:480
	s_waitcnt lgkmcnt(4)
	v_sub_f32_e32 v81, v213, v59
	v_sub_f32_e32 v80, v213, v58
	v_sub_f32_e32 v79, v213, v57
	v_sub_f32_e32 v78, v213, v56
	v_sub_f32_e32 v77, v213, v55
	v_sub_f32_e32 v76, v213, v54
	v_mfma_f32_32x32x16_bf16 v[2:17], v[134:137], v[44:47], v[2:17]
	v_sub_f32_e32 v75, v213, v53
	v_sub_f32_e32 v74, v213, v52
	v_sub_f32_e32 v73, v213, v43
	v_sub_f32_e32 v72, v213, v42
	v_sub_f32_e32 v71, v213, v41
	v_sub_f32_e32 v70, v213, v40
	s_waitcnt lgkmcnt(0)
	v_sub_f32_e32 v65, v213, v63
	v_mfma_f32_32x32x16_bf16 v[18:33], v[134:137], v[66:69], v[18:33]
	v_sub_f32_e32 v69, v213, v39
	v_sub_f32_e32 v68, v213, v38
	v_sub_f32_e32 v67, v213, v37
	v_sub_f32_e32 v66, v213, v36
	v_sub_f32_e32 v64, v213, v62
	v_sub_f32_e32 v63, v213, v61
	v_sub_f32_e32 v62, v213, v60
	v_mfma_f32_32x32x16_bf16 v[2:17], v[138:141], v[158:161], v[2:17]
	v_sub_f32_e32 v61, v213, v193
	v_sub_f32_e32 v60, v213, v192
	v_sub_f32_e32 v59, v213, v191
	v_sub_f32_e32 v58, v213, v190
	v_sub_f32_e32 v57, v213, v249
	v_sub_f32_e32 v56, v213, v248
	v_sub_f32_e32 v55, v213, v247
	v_mfma_f32_32x32x16_bf16 v[18:33], v[138:141], v[48:51], v[18:33]
	v_sub_f32_e32 v54, v213, v246
	v_sub_f32_e32 v53, v213, v245
	v_sub_f32_e32 v52, v213, v244
	v_sub_f32_e32 v51, v213, v243
	v_sub_f32_e32 v50, v213, v242
	v_mfma_f32_32x32x16_bf16 v[2:17], v[142:145], v[150:153], v[2:17]
	v_mfma_f32_32x32x16_bf16 v[18:33], v[142:145], v[166:169], v[18:33]
	v_add_u32_e32 v48, s41, v235
	ds_read_b64_tr_b16 v[36:37], v48 offset:24576
	ds_read_b64_tr_b16 v[38:39], v48 offset:25088
	v_mfma_f32_32x32x16_bf16 v[66:81], v[186:189], v[114:117], v[66:81]
	v_add_f32_e32 v40, v98, v99
	v_add_f32_e32 v40, v100, v40
	v_add_f32_e32 v40, v101, v40
	v_add_f32_e32 v40, v102, v40
	v_add_f32_e32 v44, v103, v40
	v_cvt_pk_bf16_f32 v130, v98, v99
	v_cvt_pk_bf16_f32 v131, v100, v101
	ds_read_b64_tr_b16 v[40:41], v48 offset:28672
	ds_read_b64_tr_b16 v[42:43], v48 offset:29184
	v_mfma_f32_32x32x16_bf16 v[50:65], v[178:181], v[114:117], v[50:65]
	v_add_f32_e32 v44, v104, v44
	v_add_f32_e32 v44, v105, v44
	v_add_f32_e32 v44, v106, v44
	v_add_f32_e32 v49, v107, v44
	v_cvt_pk_bf16_f32 v132, v102, v103
	v_cvt_pk_bf16_f32 v133, v104, v105
	ds_read_b64_tr_b16 v[44:45], v48 offset:25600
	ds_read_b64_tr_b16 v[46:47], v48 offset:26112
	v_mfma_f32_32x32x16_bf16 v[66:81], v[182:185], v[118:121], v[66:81]
	v_add_f32_e32 v49, v108, v49
	v_add_f32_e32 v49, v109, v49
	v_add_f32_e32 v49, v110, v49
	v_add_f32_e32 v49, v111, v49
	v_cvt_pk_bf16_f32 v134, v106, v107
	v_cvt_pk_bf16_f32 v135, v108, v109
	ds_read_b64_tr_b16 v[98:99], v48 offset:29696
	ds_read_b64_tr_b16 v[100:101], v48 offset:30208
	v_mfma_f32_32x32x16_bf16 v[50:65], v[170:173], v[118:121], v[50:65]
	v_add_f32_e32 v49, v112, v49
	v_add_f32_e32 v49, v113, v49
	v_add_f32_e32 v49, v82, v49
	v_add_f32_e32 v49, v83, v49
	v_cvt_pk_bf16_f32 v136, v110, v111
	v_cvt_pk_bf16_f32 v137, v112, v113
	ds_read_b64_tr_b16 v[102:103], v48 offset:26624
	ds_read_b64_tr_b16 v[104:105], v48 offset:27136
	v_mfma_f32_32x32x16_bf16 v[66:81], v[174:177], v[122:125], v[66:81]
	v_add_f32_e32 v49, v84, v49
	v_add_f32_e32 v49, v85, v49
	v_add_f32_e32 v49, v86, v49
	v_add_f32_e32 v49, v87, v49
	v_cvt_pk_bf16_f32 v138, v82, v83
	v_cvt_pk_bf16_f32 v139, v84, v85
	ds_read_b64_tr_b16 v[82:83], v48 offset:30720
	ds_read_b64_tr_b16 v[84:85], v48 offset:31232
	v_mfma_f32_32x32x16_bf16 v[50:65], v[154:157], v[122:125], v[50:65]
	v_add_f32_e32 v49, v88, v49
	v_add_f32_e32 v49, v89, v49
	v_add_f32_e32 v49, v90, v49
	v_add_f32_e32 v49, v91, v49
	v_cvt_pk_bf16_f32 v140, v86, v87
	v_cvt_pk_bf16_f32 v141, v88, v89
	ds_read_b64_tr_b16 v[86:87], v48 offset:27648
	ds_read_b64_tr_b16 v[88:89], v48 offset:28160
	v_mfma_f32_32x32x16_bf16 v[66:81], v[162:165], v[126:129], v[66:81]
	v_add_f32_e32 v49, v92, v49
	v_add_f32_e32 v49, v93, v49
	v_add_f32_e32 v49, v94, v49
	v_add_f32_e32 v49, v95, v49
	v_cvt_pk_bf16_f32 v142, v90, v91
	v_cvt_pk_bf16_f32 v143, v92, v93
	ds_read_b64_tr_b16 v[90:91], v48 offset:31744
	ds_read_b64_tr_b16 v[92:93], v48 offset:32256
	v_mfma_f32_32x32x16_bf16 v[50:65], v[146:149], v[126:129], v[50:65]
	v_add_f32_e32 v48, v96, v49
	v_add_f32_e32 v48, v97, v48
	v_add_f32_e32 v48, 0, v48
	v_cvt_pk_bf16_f32 v144, v94, v95
	v_cvt_pk_bf16_f32 v145, v96, v97
	s_add_i32 s41, s53, s50
	s_mov_b32 s42, m0
	s_mov_b32 m0, s41
	s_nop 0
	global_load_lds_dwordx4 v[220:221], off
	s_mov_b32 m0, s42
	s_add_i32 s41, s52, s51
	s_mov_b32 s42, m0
	s_mov_b32 m0, s41
	s_nop 0
	global_load_lds_dwordx4 v[218:219], off
	s_mov_b32 m0, s42
	v_add_f32_e32 v34, v34, v48
	s_add_i32 s30, s30, 2
	v_add_u32_e32 v186, s52, v232
	ds_read_b128 v[174:177], v186
	ds_read_b128 v[166:169], v186 offset:512
	ds_read_b128 v[170:173], v186 offset:2048
	ds_read_b128 v[158:161], v186 offset:2560
	ds_read_b128 v[162:165], v186 offset:4096
	ds_read_b128 v[150:153], v186 offset:4608
	ds_read_b128 v[154:157], v186 offset:6144
	ds_read_b128 v[146:149], v186 offset:6656
	s_waitcnt vmcnt(2) lgkmcnt(0)
	s_barrier
	v_mfma_f32_32x32x16_bf16 v[2:17], v[130:133], v[36:39], v[2:17]
	v_exp_f32_e32 v66, v66
	v_exp_f32_e32 v67, v67
	v_exp_f32_e32 v68, v68
	v_exp_f32_e32 v69, v69
	v_mfma_f32_32x32x16_bf16 v[18:33], v[130:133], v[40:43], v[18:33]
	v_exp_f32_e32 v70, v70
	v_exp_f32_e32 v71, v71
	v_exp_f32_e32 v72, v72
	v_exp_f32_e32 v73, v73
	v_mfma_f32_32x32x16_bf16 v[2:17], v[134:137], v[44:47], v[2:17]
	v_exp_f32_e32 v74, v74
	v_exp_f32_e32 v75, v75
	v_exp_f32_e32 v76, v76
	v_exp_f32_e32 v77, v77
	v_mfma_f32_32x32x16_bf16 v[18:33], v[134:137], v[98:101], v[18:33]
	v_exp_f32_e32 v78, v78
	v_exp_f32_e32 v79, v79
	v_exp_f32_e32 v80, v80
	v_exp_f32_e32 v81, v81
	v_mfma_f32_32x32x16_bf16 v[2:17], v[138:141], v[102:105], v[2:17]
	v_exp_f32_e32 v50, v50
	v_exp_f32_e32 v51, v51
	v_exp_f32_e32 v52, v52
	v_exp_f32_e32 v53, v53
	v_mfma_f32_32x32x16_bf16 v[18:33], v[138:141], v[82:85], v[18:33]
	v_exp_f32_e32 v54, v54
	v_exp_f32_e32 v55, v55
	v_exp_f32_e32 v56, v56
	v_exp_f32_e32 v57, v57
	v_mfma_f32_32x32x16_bf16 v[2:17], v[142:145], v[86:89], v[2:17]
	v_exp_f32_e32 v58, v58
	v_exp_f32_e32 v59, v59
	v_exp_f32_e32 v60, v60
	v_exp_f32_e32 v61, v61
	v_mfma_f32_32x32x16_bf16 v[18:33], v[142:145], v[90:93], v[18:33]
	v_exp_f32_e32 v62, v62
	v_exp_f32_e32 v63, v63
	v_exp_f32_e32 v64, v64
	v_exp_f32_e32 v65, v65
	s_add_i32 s41, s52, 0x2000
	s_cmpk_lg_i32 s52, 0x4000
	s_cselect_b32 s53, s41, 0
	v_lshl_add_u64 v[218:219], v[218:219], 0, s[14:15]
	v_lshl_add_u64 v[220:221], v[220:221], 0, s[14:15]
	v_add_u32_e32 v35, 0x200, v35
	s_cmp_ge_i32 s30, s9
	s_mov_b32 s42, s8
	s_cbranch_scc0 .Lattn_g2_loop
.Lattn_join:
	s_add_i32 s9, s30, 1
	s_cmp_ge_i32 s9, s49
	s_cbranch_scc1 .LBB0_1742
